# attention queue: each non-scan workgroup's first unit is its static share (item = blockIdx-16), dynamic tickets start at item 240 (on top of v102)
# baseline (speedup 1.0000x reference)
.LBB0_950:
	s_waitcnt vmcnt(0)
	v_readfirstlane_b32 s38, v241
	s_addk_i32 s38, 0xf0
	v_mov_b32_e32 v48, v173
	s_nop 1
	v_permlane32_swap_b32_e32 v173, v48
	v_add_f32_e32 v48, v173, v48
	v_div_scale_f32 v49, s[14:15], v48, v48, 1.0
	v_rcp_f32_e32 v50, v49
	s_lshl_b32 s64, s23, 7
	v_lshlrev_b32_e32 v208, 2, v188
	s_mov_b64 s[14:15], 0x23c00200
	v_fma_f32 v51, -v49, v50, 1.0
	v_fmac_f32_e32 v50, v51, v50
	v_div_scale_f32 v51, vcc, 1.0, v48, 1.0
	v_mul_f32_e32 v52, v51, v50
	v_fma_f32 v53, -v49, v52, v51
	v_fmac_f32_e32 v52, v53, v50
	v_fma_f32 v49, -v49, v52, v51
	v_div_fmas_f32 v49, v49, v50, v52
	v_lshlrev_b64 v[50:51], 11, v[200:201]
	v_lshl_add_u64 v[50:51], s[8:9], 0, v[50:51]
	v_lshl_add_u64 v[50:51], v[50:51], 0, s[64:65]
	v_div_fixup_f32 v48, v49, v48, 1.0
	v_lshl_add_u64 v[50:51], v[50:51], 0, v[208:209]
	v_lshl_add_u64 v[52:53], v[50:51], 0, s[14:15]
	v_pk_mul_f32 v[32:33], v[32:33], v[48:49] op_sel_hi:[1,0]
	v_pk_mul_f32 v[34:35], v[34:35], v[48:49] op_sel_hi:[1,0]
	v_pk_mul_f32 v[36:37], v[36:37], v[48:49] op_sel_hi:[1,0]
	v_pk_mul_f32 v[38:39], v[38:39], v[48:49] op_sel_hi:[1,0]
	v_cvt_pk_bf16_f32 v32, v32, v33
	v_cvt_pk_bf16_f32 v33, v34, v35
	v_cvt_pk_bf16_f32 v34, v36, v37
	v_cvt_pk_bf16_f32 v35, v38, v39
	v_pk_mul_f32 v[16:17], v[16:17], v[48:49] op_sel_hi:[1,0]
	v_pk_mul_f32 v[18:19], v[18:19], v[48:49] op_sel_hi:[1,0]
	v_pk_mul_f32 v[20:21], v[20:21], v[48:49] op_sel_hi:[1,0]
	v_pk_mul_f32 v[22:23], v[22:23], v[48:49] op_sel_hi:[1,0]
	v_cvt_pk_bf16_f32 v16, v16, v17
	v_cvt_pk_bf16_f32 v17, v18, v19
	v_cvt_pk_bf16_f32 v18, v20, v21
	v_cvt_pk_bf16_f32 v19, v22, v23
	v_permlane32_swap_b32_e32 v32, v34
	v_permlane32_swap_b32_e32 v33, v35
	global_store_dwordx4 v[52:53], v[32:35], off
	v_pk_mul_f32 v[40:41], v[40:41], v[48:49] op_sel_hi:[1,0]
	v_pk_mul_f32 v[42:43], v[42:43], v[48:49] op_sel_hi:[1,0]
	v_pk_mul_f32 v[44:45], v[44:45], v[48:49] op_sel_hi:[1,0]
	v_pk_mul_f32 v[46:47], v[46:47], v[48:49] op_sel_hi:[1,0]
	v_cvt_pk_bf16_f32 v40, v40, v41
	v_cvt_pk_bf16_f32 v41, v42, v43
	v_cvt_pk_bf16_f32 v42, v44, v45
	v_cvt_pk_bf16_f32 v43, v46, v47
	v_permlane32_swap_b32_e32 v16, v18
	v_permlane32_swap_b32_e32 v17, v19
	global_store_dwordx4 v[52:53], v[16:19], off offset:64
	v_pk_mul_f32 v[24:25], v[24:25], v[48:49] op_sel_hi:[1,0]
	v_pk_mul_f32 v[26:27], v[26:27], v[48:49] op_sel_hi:[1,0]
	v_pk_mul_f32 v[28:29], v[28:29], v[48:49] op_sel_hi:[1,0]
	v_pk_mul_f32 v[30:31], v[30:31], v[48:49] op_sel_hi:[1,0]
	v_cvt_pk_bf16_f32 v24, v24, v25
	v_cvt_pk_bf16_f32 v25, v26, v27
	v_cvt_pk_bf16_f32 v26, v28, v29
	v_cvt_pk_bf16_f32 v27, v30, v31
	v_permlane32_swap_b32_e32 v40, v42
	v_permlane32_swap_b32_e32 v41, v43
	global_store_dwordx4 v[52:53], v[40:43], off offset:32
	s_mov_b64 s[14:15], 0
	s_nop 1
	v_permlane32_swap_b32_e32 v24, v26
	v_permlane32_swap_b32_e32 v25, v27
	global_store_dwordx4 v[52:53], v[24:27], off offset:96

.Lpop_cold:
	s_cmp_lt_u32 s95, 16
	s_cbranch_scc1 .Lpop_cold_atomic
	s_sub_i32 s16, s95, 16
	v_mov_b32_e32 v16, s16
	v_mov_b32_e32 v17, s48
	ds_write_b32 v17, v16
	s_branch .LBB0_956

.LBB0_955:
	s_or_b64 exec, exec, s[16:17]
	s_waitcnt vmcnt(0)
	v_readfirstlane_b32 s16, v17
	v_mov_b32_e32 v17, s48
	s_nop 0
	v_add_u32_e32 v16, s16, v16
	v_add_u32_e32 v16, 0xf0, v16
	ds_write_b32 v17, v16
